# speedup vs baseline: 1.0364x; 1.0327x over previous
.LBB0_3:
	s_or_b64 exec, exec, s[6:7]
	v_lshrrev_b32_e32 v26, 3, v0
	v_lshlrev_b32_e32 v41, 2, v26
	s_waitcnt lgkmcnt(0)
	s_barrier
	global_load_dword v34, v41, s[8:9]
	global_load_dword v40, v41, s[10:11]
	v_lshlrev_b32_e32 v19, 3, v0
	v_and_b32_e32 v28, 56, v19
	v_lshlrev_b32_e32 v61, 2, v28
	v_mad_u32_u24 v19, v26, s3, v61
	ds_read2_b32 v[46:47], v19 offset1:1
	ds_read_b128 v[20:23], v61 offset:17664
	ds_read_b128 v[36:39], v61 offset:17680
	ds_read2_b32 v[52:53], v19 offset0:2 offset1:3
	ds_read2_b32 v[58:59], v19 offset0:6 offset1:7
	s_lshl_b32 s6, s18, 21
	s_waitcnt lgkmcnt(3)
	v_pk_add_f32 v[50:51], v[46:47], v[20:21] neg_lo:[0,1] neg_hi:[0,1]
	ds_read_b128 v[46:49], v61 offset:17920
	s_waitcnt lgkmcnt(2)
	v_pk_add_f32 v[52:53], v[52:53], v[22:23] neg_lo:[0,1] neg_hi:[0,1]
	s_lshl_b32 s4, s20, 1
	s_waitcnt lgkmcnt(1)
	v_pk_add_f32 v[58:59], v[58:59], v[38:39] neg_lo:[0,1] neg_hi:[0,1]
	s_add_u32 s4, s12, s4
	s_waitcnt lgkmcnt(0)
	v_pk_mul_f32 v[50:51], v[50:51], v[46:47]
	v_pk_mul_f32 v[52:53], v[52:53], v[48:49]
	s_addc_u32 s5, s13, 0
	v_lshlrev_b32_e32 v32, 1, v28
	v_mov_b32_e32 v33, v31
	v_lshl_add_u64 v[24:25], s[4:5], 0, v[32:33]
	v_mul_u32_u24_e32 v60, 0x104, v26
	v_mov_b32_e32 v27, v31
	s_lshl_b64 s[4:5], s[18:19], 14
	s_or_b64 s[4:5], s[4:5], s[20:21]
	v_add_u32_e32 v1, v30, v1
	ds_read_b128 v[54:57], v61 offset:17936
	s_waitcnt lgkmcnt(0)
	v_pk_mul_f32 v[58:59], v[58:59], v[56:57]
	s_waitcnt vmcnt(0)
	v_pk_fma_f32 v[50:51], v[34:35], v[50:51], v[40:41] op_sel_hi:[0,1,0]
	v_pk_fma_f32 v[52:53], v[34:35], v[52:53], v[40:41] op_sel_hi:[0,1,0]
	v_cvt_pk_f16_f32 v50, v50, v51
	v_cvt_pk_f16_f32 v51, v52, v53
	ds_read2_b32 v[52:53], v19 offset0:4 offset1:5
	s_waitcnt lgkmcnt(0)
	v_pk_add_f32 v[52:53], v[52:53], v[36:37] neg_lo:[0,1] neg_hi:[0,1]
	s_nop 0
	v_pk_mul_f32 v[52:53], v[52:53], v[54:55]
	s_nop 0
	v_pk_fma_f32 v[52:53], v[34:35], v[52:53], v[40:41] op_sel_hi:[0,1,0]
	v_pk_fma_f32 v[34:35], v[34:35], v[58:59], v[40:41] op_sel_hi:[0,1,0]
	v_cvt_pk_f16_f32 v52, v52, v53
	v_cvt_pk_f16_f32 v53, v34, v35
	v_lshl_or_b32 v34, v26, 15, s6
	v_mov_b32_e32 v35, v31
	v_lshl_add_u64 v[34:35], v[24:25], 0, v[34:35]
	global_store_dwordx4 v[34:35], v[50:53], off
	v_lshrrev_b32_e32 v34, 3, v18
	v_lshlrev_b32_e32 v29, 2, v34
	global_load_dword v40, v29, s[8:9]
	global_load_dword v42, v29, s[10:11]
	v_mad_u32_u24 v50, v34, s3, v61
	ds_read2_b32 v[18:19], v50 offset1:1
	v_mov_b32_e32 v35, v31
	s_waitcnt lgkmcnt(0)
	v_pk_add_f32 v[18:19], v[18:19], v[20:21] neg_lo:[0,1] neg_hi:[0,1]
	ds_read2_b32 v[20:21], v50 offset0:2 offset1:3
	v_pk_mul_f32 v[18:19], v[18:19], v[46:47]
	s_waitcnt lgkmcnt(0)
	v_pk_add_f32 v[20:21], v[20:21], v[22:23] neg_lo:[0,1] neg_hi:[0,1]
	s_nop 0
	v_pk_mul_f32 v[20:21], v[20:21], v[48:49]
	ds_read2_b32 v[22:23], v50 offset0:6 offset1:7
	s_waitcnt lgkmcnt(0)
	v_pk_add_f32 v[22:23], v[22:23], v[38:39] neg_lo:[0,1] neg_hi:[0,1]
	ds_read2st64_b32 v[38:39], v41 offset0:69 offset1:70
	v_pk_mul_f32 v[22:23], v[22:23], v[56:57]
	s_waitcnt vmcnt(0)
	v_pk_fma_f32 v[18:19], v[40:41], v[18:19], v[42:43] op_sel_hi:[0,1,0]
	v_pk_fma_f32 v[20:21], v[40:41], v[20:21], v[42:43] op_sel_hi:[0,1,0]
	v_cvt_pk_f16_f32 v18, v18, v19
	v_cvt_pk_f16_f32 v19, v20, v21
	ds_read2_b32 v[20:21], v50 offset0:4 offset1:5
	v_pk_fma_f32 v[22:23], v[40:41], v[22:23], v[42:43] op_sel_hi:[0,1,0]
	s_waitcnt lgkmcnt(0)
	v_pk_add_f32 v[20:21], v[20:21], v[36:37] neg_lo:[0,1] neg_hi:[0,1]
	s_nop 0
	v_pk_mul_f32 v[20:21], v[20:21], v[54:55]
	v_lshl_add_u64 v[36:37], s[14:15], 0, v[32:33]
	v_pk_fma_f32 v[20:21], v[40:41], v[20:21], v[42:43] op_sel_hi:[0,1,0]
	v_cvt_pk_f16_f32 v20, v20, v21
	v_cvt_pk_f16_f32 v21, v22, v23
	v_lshl_or_b32 v22, v34, 15, s6
	v_mov_b32_e32 v23, v31
	v_lshl_add_u64 v[22:23], v[24:25], 0, v[22:23]
	global_store_dwordx4 v[22:23], v[18:21], off
	v_mov_b32_e32 v40, v39
	s_nop 0
	v_lshlrev_b32_e32 v18, 8, v26
	v_sub_u32_e32 v41, v60, v18
	v_mad_u32_u24 v31, v28, s3, v41
	ds_read2_b32 v[18:19], v31 offset1:65
	v_lshl_add_u64 v[26:27], s[4:5], 0, v[26:27]
	s_waitcnt lgkmcnt(0)
	v_pk_add_f32 v[18:19], v[18:19], v[38:39] op_sel_hi:[1,0] neg_lo:[0,1] neg_hi:[0,1]
	s_nop 0
	v_pk_mul_f32 v[46:47], v[40:41], v[18:19] op_sel_hi:[0,1]
	global_load_dwordx4 v[18:21], v61, s[8:9] offset:16
	global_load_dwordx4 v[52:55], v61, s[8:9]
	global_load_dwordx4 v[22:25], v61, s[10:11] offset:16
	global_load_dwordx4 v[56:59], v61, s[10:11]
	v_mov_b32_e32 v39, 0x208
	v_mad_u32_u24 v64, v28, s3, v39
	s_waitcnt vmcnt(0)
	v_pk_fma_f32 v[46:47], v[52:53], v[46:47], v[56:57]
	s_nop 0
	v_cvt_pk_f16_f32 v60, v46, v47
	v_add_u32_e32 v47, 0x200, v31
	v_add_u32_e32 v46, v41, v64
	ds_read2_b32 v[50:51], v47 offset0:67 offset1:197
	ds_read_b32 v48, v46
	s_waitcnt lgkmcnt(1)
	v_mov_b32_e32 v49, v50
	s_waitcnt lgkmcnt(0)
	v_pk_add_f32 v[48:49], v[48:49], v[38:39] op_sel_hi:[1,0] neg_lo:[0,1] neg_hi:[0,1]
	v_mov_b32_e32 v39, 0x410
	v_pk_mul_f32 v[48:49], v[40:41], v[48:49] op_sel_hi:[0,1]
	v_pk_fma_f32 v[48:49], v[54:55], v[48:49], v[58:59]
	v_mad_u32_u24 v65, v28, s3, v39
	v_cvt_pk_f16_f32 v61, v48, v49
	v_add_u32_e32 v48, v41, v65
	ds_read_b32 v50, v48
	s_waitcnt lgkmcnt(0)
	v_pk_add_f32 v[50:51], v[50:51], v[38:39] op_sel_hi:[1,0] neg_lo:[0,1] neg_hi:[0,1]
	v_mov_b32_e32 v39, 0x618
	v_pk_mul_f32 v[50:51], v[40:41], v[50:51] op_sel_hi:[0,1]
	v_mad_u32_u24 v66, v28, s3, v39
	v_pk_fma_f32 v[50:51], v[18:19], v[50:51], v[22:23]
	v_add_u32_e32 v49, v41, v66
	v_cvt_pk_f16_f32 v62, v50, v51
	ds_read_b32 v50, v49
	ds_read_b32 v51, v31 offset:1820
	s_waitcnt lgkmcnt(0)
	v_pk_add_f32 v[38:39], v[50:51], v[38:39] op_sel_hi:[1,0] neg_lo:[0,1] neg_hi:[0,1]
	s_nop 0
	v_pk_mul_f32 v[38:39], v[40:41], v[38:39] op_sel_hi:[0,1]
	v_pk_fma_f32 v[38:39], v[20:21], v[38:39], v[24:25]
	v_mad_u32_u24 v50, v28, s3, v29
	v_cvt_pk_f16_f32 v63, v38, v39
	v_lshlrev_b64 v[38:39], 7, v[26:27]
	v_lshl_add_u64 v[26:27], v[36:37], 0, v[38:39]
	global_store_dwordx4 v[26:27], v[60:63], off sc1
	ds_read2st64_b32 v[40:41], v29 offset0:69 offset1:70
	ds_read2_b32 v[26:27], v50 offset1:65
	v_add_u32_e32 v51, 0x200, v50
	s_waitcnt lgkmcnt(1)
	v_mov_b32_e32 v42, v41
	s_waitcnt lgkmcnt(0)
	v_pk_add_f32 v[26:27], v[26:27], v[40:41] op_sel_hi:[1,0] neg_lo:[0,1] neg_hi:[0,1]
	v_add_u32_e32 v41, v29, v64
	v_pk_mul_f32 v[26:27], v[42:43], v[26:27] op_sel_hi:[0,1]
	v_pk_fma_f32 v[26:27], v[52:53], v[26:27], v[56:57]
	ds_read2_b32 v[56:57], v51 offset0:67 offset1:197
	ds_read_b32 v52, v41
	v_cvt_pk_f16_f32 v26, v26, v27
	s_waitcnt lgkmcnt(1)
	v_mov_b32_e32 v53, v56
	s_waitcnt lgkmcnt(0)
	v_pk_add_f32 v[52:53], v[52:53], v[40:41] op_sel_hi:[1,0] neg_lo:[0,1] neg_hi:[0,1]
	s_nop 0
	v_pk_mul_f32 v[52:53], v[42:43], v[52:53] op_sel_hi:[0,1]
	v_pk_fma_f32 v[52:53], v[54:55], v[52:53], v[58:59]
	v_add_u32_e32 v54, v29, v65
	ds_read_b32 v56, v54
	v_cvt_pk_f16_f32 v27, v52, v53
	s_waitcnt lgkmcnt(0)
	v_pk_add_f32 v[52:53], v[56:57], v[40:41] op_sel_hi:[1,0] neg_lo:[0,1] neg_hi:[0,1]
	s_nop 0
	v_pk_mul_f32 v[52:53], v[42:43], v[52:53] op_sel_hi:[0,1]
	v_pk_fma_f32 v[18:19], v[18:19], v[52:53], v[22:23]
	v_add_u32_e32 v22, v29, v66
	v_cvt_pk_f16_f32 v28, v18, v19
	ds_read_b32 v18, v22
	ds_read_b32 v19, v50 offset:1820
	s_waitcnt lgkmcnt(0)
	v_pk_add_f32 v[18:19], v[18:19], v[40:41] op_sel_hi:[1,0] neg_lo:[0,1] neg_hi:[0,1]
	s_nop 0
	v_pk_mul_f32 v[18:19], v[42:43], v[18:19] op_sel_hi:[0,1]
	v_pk_fma_f32 v[18:19], v[20:21], v[18:19], v[24:25]
	s_nop 0
	v_cvt_pk_f16_f32 v29, v18, v19
	v_lshl_add_u64 v[18:19], s[4:5], 0, v[34:35]
	v_lshlrev_b64 v[18:19], 7, v[18:19]
	v_lshl_add_u64 v[20:21], v[36:37], 0, v[18:19]
	global_store_dwordx4 v[20:21], v[26:29], off sc1
	s_barrier
	ds_write2_b32 v1, v14, v15 offset1:1
	ds_write2_b32 v1, v16, v17 offset0:2 offset1:3
	v_add_u32_e32 v1, v30, v44
	ds_write2_b32 v1, v10, v11 offset1:1
	ds_write2_b32 v1, v12, v13 offset0:2 offset1:3
	v_add_u32_e32 v1, v30, v43
	ds_write2_b32 v1, v6, v7 offset1:1
	ds_write2_b32 v1, v8, v9 offset0:2 offset1:3
	v_add_u32_e32 v1, v30, v45
	ds_write2_b32 v1, v2, v3 offset1:1
	ds_write2_b32 v1, v4, v5 offset0:2 offset1:3
	s_waitcnt lgkmcnt(0)
	s_barrier
	ds_read2_b32 v[8:9], v31 offset1:65
	ds_read_b32 v1, v46
	ds_read2_b32 v[2:3], v47 offset0:67 offset1:197
	ds_read_b32 v4, v48
	ds_read_b32 v5, v49
	ds_read_b32 v10, v31 offset:1820
	v_lshl_add_u64 v[6:7], s[16:17], 0, v[32:33]
	s_mov_b64 s[4:5], 0
	s_waitcnt lgkmcnt(2)
	v_cvt_pk_f16_f32 v4, v4, v3
	v_cvt_pk_f16_f32 v3, v1, v2
	s_waitcnt lgkmcnt(0)
	v_cvt_pk_f16_f32 v5, v5, v10
	v_cvt_pk_f16_f32 v2, v8, v9
	v_lshl_add_u64 v[8:9], v[6:7], 0, v[38:39]
	global_store_dwordx4 v[8:9], v[2:5], off sc1
	ds_read2_b32 v[8:9], v50 offset1:65
	ds_read_b32 v1, v41
	ds_read2_b32 v[2:3], v51 offset0:67 offset1:197
	ds_read_b32 v4, v54
	ds_read_b32 v5, v22
	ds_read_b32 v10, v50 offset:1820
	v_lshl_add_u64 v[6:7], v[6:7], 0, v[18:19]
	s_waitcnt lgkmcnt(2)
	v_cvt_pk_f16_f32 v4, v4, v3
	v_cvt_pk_f16_f32 v3, v1, v2
	s_waitcnt lgkmcnt(0)
	v_cvt_pk_f16_f32 v5, v5, v10
	v_cvt_pk_f16_f32 v2, v8, v9
	global_store_dwordx4 v[6:7], v[2:5], off sc1

.LBB1_23:
	v_mul_u32_u24_e32 v4, 0xf83f, v12
	v_lshrrev_b32_e32 v4, 23, v4
	v_cmp_lt_u32_e32 vcc, s8, v12
	v_mad_i32_i24 v6, v4, s3, v12
	v_add_u32_e32 v5, 0x400, v12
	s_or_b64 s[0:1], vcc, s[0:1]
	v_cmp_lt_i32_e32 vcc, s6, v6
	v_mov_b32_e32 v12, v5
	s_nop 0
	v_cndmask_b32_e32 v5, 0, v1, vcc
	v_cndmask_b32_e32 v7, 0, v2, vcc
	v_add_lshl_u32 v5, v6, v5, 2
	v_cndmask_b32_e32 v6, 0, v3, vcc
	v_lshl_add_u32 v7, v4, 2, v7
	v_lshl_add_u32 v4, v4, 3, v6
	v_mul_u32_u24_e32 v6, 0x10c, v7
	v_add_u32_e32 v7, 0x42, v7
	v_mul_u32_u24_e32 v4, 0x43, v4
	v_add3_u32 v8, v6, v5, s2
	v_mul_u32_u24_e32 v6, 0x10c, v7
	v_lshl_add_u32 v13, v4, 2, v5
	v_add3_u32 v18, v6, v5, s2
	ds_read2_b32 v[4:5], v8 offset1:67
	ds_read2_b32 v[6:7], v8 offset0:134 offset1:201
	v_add_u32_e32 v16, 0x400, v8
	ds_read2_b32 v[8:9], v18 offset1:67
	ds_read2_b32 v[10:11], v18 offset0:134 offset1:201
	ds_read2_b32 v[16:17], v16 offset0:12 offset1:79
	v_add_u32_e32 v18, 0x400, v18
	ds_read2_b32 v[18:19], v18 offset0:12 offset1:79
	s_waitcnt lgkmcnt(5)
	v_mul_f32_e32 v21, 0x3daefbd6, v4
	s_waitcnt lgkmcnt(4)
	v_mul_f32_e32 v24, 0xbe0a4054, v6
	v_mul_f32_e32 v25, 0x3daefbd6, v6
	v_mul_f32_e32 v22, 0xbe0a4054, v5
	v_mul_f32_e32 v23, 0x3daefbd6, v5
	v_mul_f32_e32 v27, 0x3daefbd6, v7
	v_fma_f32 v21, v5, s7, -v21
	v_fmac_f32_e32 v24, 0x3d104972, v5
	v_fma_f32 v5, v7, s7, -v25
	s_waitcnt lgkmcnt(1)
	v_mul_f32_e32 v25, 0xbe0a4054, v16
	v_mul_f32_e32 v26, 0xbe0a4054, v7
	v_fmac_f32_e32 v22, 0x3d104972, v4
	v_fma_f32 v4, v6, s7, -v23
	v_fma_f32 v23, v16, s7, -v27
	v_fmac_f32_e32 v25, 0x3d104972, v7
	v_fmac_f32_e32 v26, 0x3d104972, v6
	v_fmac_f32_e32 v21, 0x3eaa53cb, v6
	v_fmac_f32_e32 v22, 0x3f4e9071, v6
	v_fmac_f32_e32 v23, 0x3eaa53cb, v17
	v_fmac_f32_e32 v25, 0x3f4e9071, v17
	v_fmac_f32_e32 v4, 0x3eaa53cb, v7
	v_fmac_f32_e32 v24, 0x3f4e9071, v7
	v_fmac_f32_e32 v5, 0x3eaa53cb, v16
	v_fmac_f32_e32 v26, 0x3f4e9071, v16
	v_fmac_f32_e32 v21, 0x3f4e9071, v8
	v_fmac_f32_e32 v22, 0xbeaa53cb, v8
	v_fmac_f32_e32 v23, 0x3f4e9071, v11
	v_fmac_f32_e32 v25, 0xbeaa53cb, v11
	v_fmac_f32_e32 v4, 0x3f4e9071, v9
	v_fmac_f32_e32 v24, 0xbeaa53cb, v9
	v_fmac_f32_e32 v5, 0x3f4e9071, v10
	v_fmac_f32_e32 v26, 0xbeaa53cb, v10
	v_fmac_f32_e32 v21, 0xbe0a4054, v9
	v_fmac_f32_e32 v22, 0xbeeb7510, v9
	s_waitcnt lgkmcnt(0)
	v_fmac_f32_e32 v23, 0xbe0a4054, v18
	v_fmac_f32_e32 v25, 0xbeeb7510, v18
	v_add_u32_e32 v20, 0x400, v13
	v_fmac_f32_e32 v4, 0xbe0a4054, v10
	v_fmac_f32_e32 v24, 0xbeeb7510, v10
	v_fmac_f32_e32 v5, 0xbe0a4054, v11
	v_fmac_f32_e32 v26, 0xbeeb7510, v11
	v_fmac_f32_e32 v21, 0x3d104972, v10
	v_fmac_f32_e32 v22, 0x3daefbd6, v10
	v_fmac_f32_e32 v23, 0x3d104972, v19
	v_fmac_f32_e32 v25, 0x3daefbd6, v19
	v_fmac_f32_e32 v4, 0x3d104972, v11
	v_fmac_f32_e32 v24, 0x3daefbd6, v11
	v_fmac_f32_e32 v5, 0x3d104972, v18
	v_fmac_f32_e32 v26, 0x3daefbd6, v18
	ds_write2_b32 v13, v21, v22 offset1:67
	ds_write2_b32 v13, v4, v24 offset0:134 offset1:201
	ds_write2_b32 v20, v5, v26 offset0:12 offset1:79
	ds_write2_b32 v20, v23, v25 offset0:146 offset1:213
	s_andn2_b64 exec, exec, s[0:1]
	s_cbranch_execnz .LBB1_23
	s_or_b64 exec, exec, s[0:1]
	v_and_b32_e32 v0, 15, v0
	s_lshl_b64 s[0:1], s[4:5], 1
	s_add_u32 s0, s10, s0
	v_lshlrev_b32_e32 v0, 4, v0
	s_movk_i32 s10, 0x10c
	v_mad_u32_u24 v12, v15, s10, v0
	v_add_u32_e32 v4, 0x8608, v12
	s_waitcnt lgkmcnt(0)
	s_barrier
	ds_read2_b32 v[4:5], v4 offset1:1
	ds_read2_b32 v[10:11], v12 offset1:1
	v_add_u32_e32 v6, 0x8600, v12
	s_addc_u32 s1, s11, s1
	v_mov_b32_e32 v1, 0
	v_add_u32_e32 v19, 0x8610, v12
	ds_read2_b32 v[8:9], v6 offset1:1
	ds_read2_b32 v[6:7], v12 offset0:4 offset1:5
	ds_read2_b32 v[12:13], v12 offset0:2 offset1:3
	v_lshl_add_u64 v[2:3], s[0:1], 0, v[0:1]
	s_mov_b32 s0, 0x3d104972
	s_mov_b32 s1, 0x3eeb7510
	s_mov_b32 s2, 0x3daefbd6
	s_mov_b32 s4, 0x3f4e9071
	s_waitcnt lgkmcnt(3)
	v_pk_mul_f32 v[16:17], v[10:11], s[0:1]
	s_mov_b32 s3, 0x3e0a4054
	s_mov_b32 s5, 0x3eaa53cb
	v_pk_fma_f32 v[16:17], v[10:11], s[2:3], v[16:17] op_sel:[0,0,1] op_sel_hi:[1,1,0] neg_lo:[1,0,0] neg_hi:[1,0,0]
	v_mad_u32_u24 v28, v14, s10, v0
	s_mov_b32 s10, s5
	s_mov_b32 s11, s4
	s_waitcnt lgkmcnt(0)
	v_pk_fma_f32 v[16:17], v[12:13], s[10:11], v[16:17] op_sel_hi:[0,1,1]
	v_pk_fma_f32 v[26:27], v[8:9], s[4:5], v[16:17]
	v_pk_fma_f32 v[16:17], v[8:9], s[4:5], v[16:17] op_sel_hi:[0,1,1] neg_lo:[1,0,0] neg_hi:[1,0,0]
	s_mov_b32 s6, s3
	s_mov_b32 s7, s1
	v_mov_b32_e32 v27, v17
	v_pk_fma_f32 v[16:17], v[8:9], s[6:7], v[26:27] op_sel:[1,0,0] neg_lo:[1,0,0] neg_hi:[1,0,0]
	v_mov_b32_e32 v27, v11
	v_pk_mov_b32 v[10:11], v[10:11], v[12:13] op_sel:[1,0]
	v_mov_b32_e32 v26, v12
	s_mov_b32 s12, s1
	s_mov_b32 s13, s0
	v_pk_mul_f32 v[10:11], v[10:11], s[2:3]
	v_mov_b32_e32 v18, v9
	v_pk_fma_f32 v[10:11], v[26:27], s[12:13], v[10:11] neg_lo:[0,0,1] neg_hi:[0,0,1]
	ds_read2_b32 v[20:21], v19 offset1:1
	ds_read2_b32 v[22:23], v28 offset1:1
	ds_read2_b32 v[24:25], v28 offset0:2 offset1:3
	v_pk_fma_f32 v[10:11], v[12:13], s[10:11], v[10:11] op_sel:[1,0,0]
	s_mov_b32 s8, s0
	v_pk_fma_f32 v[18:19], v[18:19], s[4:5], v[10:11]
	v_pk_fma_f32 v[8:9], v[8:9], s[4:5], v[10:11] op_sel:[1,0,0] neg_lo:[1,0,0] neg_hi:[1,0,0]
	s_mov_b32 s9, s2
	v_mov_b32_e32 v19, v9
	v_pk_fma_f32 v[8:9], v[4:5], s[6:7], v[18:19] op_sel_hi:[0,1,1] neg_lo:[1,0,0] neg_hi:[1,0,0]
	v_pk_fma_f32 v[16:17], v[4:5], s[8:9], v[16:17] op_sel_hi:[0,1,1]
	v_pk_fma_f32 v[8:9], v[4:5], s[8:9], v[8:9] op_sel:[1,0,0]
	v_cvt_pk_f16_f32 v16, v16, v17
	v_cvt_pk_f16_f32 v17, v8, v9
	v_pk_mul_f32 v[8:9], v[12:13], s[0:1]
	v_mov_b32_e32 v0, v5
	v_pk_fma_f32 v[8:9], v[12:13], s[2:3], v[8:9] op_sel:[0,0,1] op_sel_hi:[1,1,0] neg_lo:[1,0,0] neg_hi:[1,0,0]
	v_mov_b32_e32 v12, v6
	v_pk_fma_f32 v[8:9], v[6:7], s[10:11], v[8:9] op_sel_hi:[0,1,1]
	v_pk_fma_f32 v[10:11], v[4:5], s[4:5], v[8:9]
	v_pk_fma_f32 v[8:9], v[4:5], s[4:5], v[8:9] op_sel_hi:[0,1,1] neg_lo:[1,0,0] neg_hi:[1,0,0]
	v_mov_b32_e32 v11, v9
	v_pk_fma_f32 v[8:9], v[4:5], s[6:7], v[10:11] op_sel:[1,0,0] neg_lo:[1,0,0] neg_hi:[1,0,0]
	s_waitcnt lgkmcnt(2)
	v_pk_fma_f32 v[8:9], v[20:21], s[8:9], v[8:9] op_sel_hi:[0,1,1]
	v_cvt_pk_f16_f32 v18, v8, v9
	v_mov_b32_e32 v8, v13
	v_mov_b32_e32 v9, v6
	v_pk_mul_f32 v[8:9], v[8:9], s[2:3]
	s_nop 0
	v_pk_fma_f32 v[8:9], v[12:13], s[12:13], v[8:9] neg_lo:[0,0,1] neg_hi:[0,0,1]
	s_nop 0
	v_pk_fma_f32 v[6:7], v[6:7], s[10:11], v[8:9] op_sel:[1,0,0]
	s_nop 0
	v_pk_fma_f32 v[8:9], v[0:1], s[4:5], v[6:7]
	v_pk_fma_f32 v[4:5], v[4:5], s[4:5], v[6:7] op_sel:[1,0,0] neg_lo:[1,0,0] neg_hi:[1,0,0]
	v_add_u32_e32 v0, 0x8600, v28
	v_mov_b32_e32 v9, v5
	v_pk_fma_f32 v[4:5], v[20:21], s[6:7], v[8:9] op_sel_hi:[0,1,1] neg_lo:[1,0,0] neg_hi:[1,0,0]
	v_pk_fma_f32 v[4:5], v[20:21], s[8:9], v[4:5] op_sel:[1,0,0]
	s_waitcnt lgkmcnt(0)
	v_pk_mov_b32 v[20:21], v[22:23], v[24:25] op_sel:[1,0]
	v_cvt_pk_f16_f32 v19, v4, v5
	v_lshlrev_b32_e32 v4, 8, v15
	v_mov_b32_e32 v5, v1
	v_lshl_add_u64 v[4:5], v[2:3], 0, v[4:5]
	global_store_dwordx4 v[4:5], v[16:19], off sc1
	v_add_u32_e32 v4, 0x8608, v28
	v_add_u32_e32 v5, 0x8610, v28
	ds_read2_b32 v[6:7], v0 offset1:1
	ds_read2_b32 v[8:9], v4 offset1:1
	ds_read2_b32 v[10:11], v5 offset1:1
	ds_read2_b32 v[12:13], v28 offset0:4 offset1:5
	v_pk_mul_f32 v[4:5], v[22:23], s[0:1]
	v_pk_mul_f32 v[20:21], v[20:21], s[2:3]
	v_pk_fma_f32 v[4:5], v[22:23], s[2:3], v[4:5] op_sel:[0,0,1] op_sel_hi:[1,1,0] neg_lo:[1,0,0] neg_hi:[1,0,0]
	s_waitcnt lgkmcnt(3)
	v_mov_b32_e32 v0, v7
	v_pk_fma_f32 v[4:5], v[24:25], s[10:11], v[4:5] op_sel_hi:[0,1,1]
	v_pk_fma_f32 v[18:19], v[6:7], s[4:5], v[4:5]
	v_pk_fma_f32 v[4:5], v[6:7], s[4:5], v[4:5] op_sel_hi:[0,1,1] neg_lo:[1,0,0] neg_hi:[1,0,0]
	v_mov_b32_e32 v19, v5
	v_pk_fma_f32 v[4:5], v[6:7], s[6:7], v[18:19] op_sel:[1,0,0] neg_lo:[1,0,0] neg_hi:[1,0,0]
	v_mov_b32_e32 v18, v24
	v_mov_b32_e32 v19, v23
	v_pk_fma_f32 v[18:19], v[18:19], s[12:13], v[20:21] neg_lo:[0,0,1] neg_hi:[0,0,1]
	s_waitcnt lgkmcnt(2)
	v_pk_fma_f32 v[4:5], v[8:9], s[8:9], v[4:5] op_sel_hi:[0,1,1]
	v_pk_fma_f32 v[18:19], v[24:25], s[10:11], v[18:19] op_sel:[1,0,0]
	v_cvt_pk_f16_f32 v4, v4, v5
	v_pk_fma_f32 v[20:21], v[0:1], s[4:5], v[18:19]
	v_pk_fma_f32 v[6:7], v[6:7], s[4:5], v[18:19] op_sel:[1,0,0] neg_lo:[1,0,0] neg_hi:[1,0,0]
	v_mov_b32_e32 v16, v9
	v_mov_b32_e32 v21, v7
	v_pk_fma_f32 v[6:7], v[8:9], s[6:7], v[20:21] op_sel_hi:[0,1,1] neg_lo:[1,0,0] neg_hi:[1,0,0]
	v_pk_fma_f32 v[6:7], v[8:9], s[8:9], v[6:7] op_sel:[1,0,0]
	v_lshlrev_b32_e32 v0, 8, v14
	v_cvt_pk_f16_f32 v5, v6, v7
	v_pk_mul_f32 v[6:7], v[24:25], s[0:1]
	v_lshl_add_u64 v[0:1], v[2:3], 0, v[0:1]
	v_pk_fma_f32 v[6:7], v[24:25], s[2:3], v[6:7] op_sel:[0,0,1] op_sel_hi:[1,1,0] neg_lo:[1,0,0] neg_hi:[1,0,0]
	s_waitcnt lgkmcnt(0)
	v_mov_b32_e32 v24, v12
	v_pk_fma_f32 v[6:7], v[12:13], s[10:11], v[6:7] op_sel_hi:[0,1,1]
	v_pk_fma_f32 v[18:19], v[8:9], s[4:5], v[6:7]
	v_pk_fma_f32 v[6:7], v[8:9], s[4:5], v[6:7] op_sel_hi:[0,1,1] neg_lo:[1,0,0] neg_hi:[1,0,0]
	v_mov_b32_e32 v19, v7
	v_pk_fma_f32 v[6:7], v[8:9], s[6:7], v[18:19] op_sel:[1,0,0] neg_lo:[1,0,0] neg_hi:[1,0,0]
	v_mov_b32_e32 v18, v25
	v_mov_b32_e32 v19, v12
	v_pk_mul_f32 v[18:19], v[18:19], s[2:3]
	v_pk_fma_f32 v[6:7], v[10:11], s[8:9], v[6:7] op_sel_hi:[0,1,1]
	v_pk_fma_f32 v[18:19], v[24:25], s[12:13], v[18:19] neg_lo:[0,0,1] neg_hi:[0,0,1]
	v_cvt_pk_f16_f32 v6, v6, v7
	v_pk_fma_f32 v[12:13], v[12:13], s[10:11], v[18:19] op_sel:[1,0,0]
	s_nop 0
	v_pk_fma_f32 v[16:17], v[16:17], s[4:5], v[12:13]
	v_pk_fma_f32 v[8:9], v[8:9], s[4:5], v[12:13] op_sel:[1,0,0] neg_lo:[1,0,0] neg_hi:[1,0,0]
	s_nop 0
	v_mov_b32_e32 v17, v9
	v_pk_fma_f32 v[8:9], v[10:11], s[6:7], v[16:17] op_sel_hi:[0,1,1] neg_lo:[1,0,0] neg_hi:[1,0,0]
	v_pk_fma_f32 v[8:9], v[10:11], s[8:9], v[8:9] op_sel:[1,0,0]
	s_nop 0
	v_cvt_pk_f16_f32 v7, v8, v9
	global_store_dwordx4 v[0:1], v[4:7], off sc1
	s_endpgm

.LBB2_10:
	s_waitcnt vmcnt(11)
	v_mfma_f32_16x16x32_f16 v[74:77], v[66:69], v[18:21], 0
	s_cmp_lt_u32 s25, 2
	s_cselect_b64 s[14:15], -1, 0
	s_cmp_gt_u32 s25, 1
	s_waitcnt vmcnt(9)
	v_mfma_f32_16x16x32_f16 v[102:105], v[58:61], v[18:21], 0
	s_mov_b64 s[20:21], -1
	v_mfma_f32_16x16x32_f16 v[106:109], v[66:69], v[26:29], 0
	v_mfma_f32_16x16x32_f16 v[110:113], v[58:61], v[26:29], 0
	v_mfma_f32_16x16x32_f16 v[66:69], v[66:69], v[34:37], 0
	v_mfma_f32_16x16x32_f16 v[58:61], v[58:61], v[34:37], 0
	v_mfma_f32_16x16x32_f16 v[74:77], v[70:73], v[22:25], v[74:77]
	s_waitcnt vmcnt(8)
	v_mfma_f32_16x16x32_f16 v[102:105], v[62:65], v[22:25], v[102:105]
	v_mfma_f32_16x16x32_f16 v[106:109], v[70:73], v[30:33], v[106:109]
	s_nop 4
	v_cvt_pk_f16_f32 v77, v76, v77
	v_cvt_pk_f16_f32 v76, v74, v75
	v_cvt_pk_f16_f32 v75, v104, v105
	v_mfma_f32_16x16x32_f16 v[110:113], v[62:65], v[30:33], v[110:113]
	v_cvt_pk_f16_f32 v74, v102, v103
	ds_write2_b64 v87, v[76:77], v[74:75] offset1:4
	v_cvt_pk_f16_f32 v75, v108, v109
	v_mfma_f32_16x16x32_f16 v[66:69], v[70:73], v[38:41], v[66:69]
	v_cvt_pk_f16_f32 v74, v106, v107
	s_nop 2
	v_cvt_pk_f16_f32 v71, v112, v113
	v_cvt_pk_f16_f32 v70, v110, v111
	v_mfma_f32_16x16x32_f16 v[58:61], v[62:65], v[38:41], v[58:61]
	ds_write2_b64 v88, v[74:75], v[70:71] offset1:4
	v_cvt_pk_f16_f32 v69, v68, v69
	v_cvt_pk_f16_f32 v68, v66, v67
	s_nop 4
	v_cvt_pk_f16_f32 v61, v60, v61
	v_cvt_pk_f16_f32 v60, v58, v59
	ds_write2_b64 v89, v[68:69], v[60:61] offset1:4
	s_waitcnt lgkmcnt(0)
	s_barrier
	v_add_u32_e32 v58, 0x10e00, v86
	ds_read_b128 v[58:61], v58
	ds_read_b128 v[62:65], v90
	ds_read_b128 v[66:69], v90 offset:15360
	ds_read_b128 v[70:73], v91
	s_waitcnt lgkmcnt(2)
	v_pk_fma_f16 v77, v58, v62, 0
	v_add_u32_e32 v62, 0x10e10, v86
	v_pk_fma_f16 v74, v61, v65, 0
	v_pk_fma_f16 v75, v60, v64, 0
	v_pk_fma_f16 v76, v59, v63, 0
	ds_read_b128 v[62:65], v62
	s_waitcnt lgkmcnt(2)
	v_pk_fma_f16 v101, v61, v69, 0
	v_pk_fma_f16 v102, v60, v68, 0
	v_pk_fma_f16 v103, v59, v67, 0
	v_pk_fma_f16 v66, v58, v66, 0
	ds_read_b128 v[58:61], v91 offset:15360
	s_waitcnt lgkmcnt(1)
	v_pk_fma_f16 v77, v62, v70, v77
	v_pk_fma_f16 v76, v63, v71, v76
	v_pk_fma_f16 v75, v64, v72, v75
	v_pk_fma_f16 v74, v65, v73, v74
	s_waitcnt lgkmcnt(0)
	v_pk_fma_f16 v104, v62, v58, v66
	v_add_u32_e32 v58, 0x10e20, v86
	ds_read_b128 v[66:69], v58
	ds_read_b128 v[70:73], v92
	v_pk_fma_f16 v103, v63, v59, v103
	v_pk_fma_f16 v102, v64, v60, v102
	v_pk_fma_f16 v101, v65, v61, v101
	ds_read_b128 v[58:61], v92 offset:15360
	v_add_u32_e32 v62, 0x10e30, v86
	s_waitcnt lgkmcnt(1)
	v_pk_fma_f16 v74, v69, v73, v74
	v_pk_fma_f16 v75, v68, v72, v75
	v_pk_fma_f16 v76, v67, v71, v76
	v_pk_fma_f16 v77, v66, v70, v77
	ds_read_b128 v[62:65], v62
	s_waitcnt lgkmcnt(1)
	v_pk_fma_f16 v101, v69, v61, v101
	ds_read_b128 v[70:73], v93
	v_pk_fma_f16 v102, v68, v60, v102
	v_pk_fma_f16 v103, v67, v59, v103
	v_pk_fma_f16 v66, v66, v58, v104
	ds_read_b128 v[58:61], v93 offset:15360
	s_waitcnt lgkmcnt(1)
	v_pk_fma_f16 v77, v62, v70, v77
	v_pk_fma_f16 v76, v63, v71, v76
	v_pk_fma_f16 v75, v64, v72, v75
	v_pk_fma_f16 v74, v65, v73, v74
	s_waitcnt lgkmcnt(0)
	v_pk_fma_f16 v104, v62, v58, v66
	v_add_u32_e32 v58, 0x10e40, v86
	ds_read_b128 v[66:69], v58
	ds_read_b128 v[70:73], v94
	v_pk_fma_f16 v103, v63, v59, v103
	v_pk_fma_f16 v102, v64, v60, v102
	v_pk_fma_f16 v101, v65, v61, v101
	ds_read_b128 v[58:61], v94 offset:15360
	v_add_u32_e32 v62, 0x10e50, v86
	s_waitcnt lgkmcnt(1)
	v_pk_fma_f16 v74, v69, v73, v74
	v_pk_fma_f16 v75, v68, v72, v75
	v_pk_fma_f16 v76, v67, v71, v76
	v_pk_fma_f16 v77, v66, v70, v77
	ds_read_b128 v[62:65], v62
	s_waitcnt lgkmcnt(1)
	v_pk_fma_f16 v101, v69, v61, v101
	ds_read_b128 v[70:73], v95
	v_pk_fma_f16 v102, v68, v60, v102
	v_pk_fma_f16 v103, v67, v59, v103
	v_pk_fma_f16 v66, v66, v58, v104
	ds_read_b128 v[58:61], v95 offset:15360
	s_waitcnt lgkmcnt(1)
	v_pk_fma_f16 v77, v62, v70, v77
	v_pk_fma_f16 v76, v63, v71, v76
	v_pk_fma_f16 v75, v64, v72, v75
	v_pk_fma_f16 v74, v65, v73, v74
	s_waitcnt lgkmcnt(0)
	v_pk_fma_f16 v104, v62, v58, v66
	v_add_u32_e32 v58, 0x10e60, v86
	ds_read_b128 v[66:69], v58
	ds_read_b128 v[70:73], v96
	v_pk_fma_f16 v103, v63, v59, v103
	v_pk_fma_f16 v102, v64, v60, v102
	v_pk_fma_f16 v101, v65, v61, v101
	ds_read_b128 v[58:61], v96 offset:15360
	v_add_u32_e32 v62, 0x10e70, v86
	s_waitcnt lgkmcnt(1)
	v_pk_fma_f16 v74, v69, v73, v74
	v_pk_fma_f16 v75, v68, v72, v75
	v_pk_fma_f16 v76, v67, v71, v76
	v_pk_fma_f16 v77, v66, v70, v77
	ds_read_b128 v[62:65], v62
	s_waitcnt lgkmcnt(1)
	v_pk_fma_f16 v101, v69, v61, v101
	ds_read_b128 v[70:73], v97
	v_pk_fma_f16 v102, v68, v60, v102
	v_pk_fma_f16 v103, v67, v59, v103
	v_pk_fma_f16 v66, v66, v58, v104
	ds_read_b128 v[58:61], v97 offset:15360
	s_waitcnt lgkmcnt(1)
	v_pk_fma_f16 v77, v62, v70, v77
	v_pk_fma_f16 v76, v63, v71, v76
	v_pk_fma_f16 v75, v64, v72, v75
	v_pk_fma_f16 v74, v65, v73, v74
	s_waitcnt lgkmcnt(0)
	v_pk_fma_f16 v104, v62, v58, v66
	v_add_u32_e32 v58, 0x10e80, v86
	ds_read_b128 v[66:69], v58
	ds_read_b128 v[70:73], v98
	v_pk_fma_f16 v103, v63, v59, v103
	v_pk_fma_f16 v102, v64, v60, v102
	v_pk_fma_f16 v101, v65, v61, v101
	ds_read_b128 v[62:65], v98 offset:15360
	s_waitcnt lgkmcnt(1)
	v_pk_fma_f16 v61, v69, v73, v74
	v_pk_fma_f16 v60, v68, v72, v75
	v_pk_fma_f16 v59, v67, v71, v76
	v_pk_fma_f16 v58, v66, v70, v77
	s_waitcnt lgkmcnt(0)
	v_pk_fma_f16 v65, v69, v65, v101
	v_pk_fma_f16 v64, v68, v64, v102
	v_pk_fma_f16 v63, v67, v63, v103
	v_pk_fma_f16 v62, v66, v62, v104
	s_cbranch_scc0 .LBB2_12
	global_store_dwordx4 v[82:83], v[58:61], off sc1
	global_store_dwordx4 v[80:81], v[62:65], off sc1
	s_mov_b64 s[20:21], 0

.LBB4_118:
	s_or_b64 exec, exec, s[0:1]
	s_waitcnt lgkmcnt(0)
	s_barrier
	s_waitcnt vmcnt(0)
	ds_read_b128 v[18:21], v75 offset:8192
	ds_read_b128 v[22:25], v74
	ds_read_b128 v[26:29], v75 offset:9216
	v_or_b32_e32 v30, s29, v98
	v_add_lshl_u32 v0, s27, v1, 9
	v_mov_b32_e32 v1, 0
	s_waitcnt lgkmcnt(1)
	v_mfma_f32_16x16x32_f16 v[2:5], v[18:21], v[22:25], v[2:5]
	ds_read_b128 v[18:21], v75 offset:10240
	s_waitcnt lgkmcnt(1)
	v_mfma_f32_16x16x32_f16 v[6:9], v[26:29], v[22:25], v[6:9]
	ds_read_b128 v[26:29], v75 offset:11264
	s_waitcnt lgkmcnt(1)
	v_mfma_f32_16x16x32_f16 v[10:13], v[18:21], v[22:25], v[10:13]
	v_lshl_add_u64 v[18:19], s[6:7], 0, v[0:1]
	v_lshlrev_b32_e32 v0, 2, v30
	v_lshl_add_u64 v[0:1], v[18:19], 0, v[0:1]
	v_lshl_add_u64 v[18:19], v[0:1], 0, v[40:41]
	global_store_dword v[18:19], v2, off sc1
	v_lshl_add_u64 v[18:19], v[0:1], 0, v[42:43]
	global_store_dword v[18:19], v3, off sc1
	v_lshl_add_u64 v[2:3], v[0:1], 0, v[44:45]
	global_store_dword v[2:3], v4, off sc1
	v_lshl_add_u64 v[2:3], v[0:1], 0, v[46:47]
	global_store_dword v[2:3], v5, off sc1
	v_lshl_add_u64 v[2:3], v[0:1], 0, v[48:49]
	global_store_dword v[2:3], v6, off sc1
	v_lshl_add_u64 v[2:3], v[0:1], 0, v[50:51]
	global_store_dword v[2:3], v7, off sc1
	v_lshl_add_u64 v[2:3], v[0:1], 0, v[52:53]
	global_store_dword v[2:3], v8, off sc1
	v_lshl_add_u64 v[2:3], v[0:1], 0, v[54:55]
	global_store_dword v[2:3], v9, off sc1
	v_lshl_add_u64 v[2:3], v[0:1], 0, v[56:57]
	s_waitcnt lgkmcnt(0)
	v_mfma_f32_16x16x32_f16 v[14:17], v[26:29], v[22:25], v[14:17]
	global_store_dword v[2:3], v10, off sc1
	v_lshl_add_u64 v[2:3], v[0:1], 0, v[58:59]
	global_store_dword v[2:3], v11, off sc1
	v_lshl_add_u64 v[2:3], v[0:1], 0, v[60:61]
	global_store_dword v[2:3], v12, off sc1
	v_lshl_add_u64 v[2:3], v[0:1], 0, v[62:63]
	global_store_dword v[2:3], v13, off sc1
	v_lshl_add_u64 v[2:3], v[0:1], 0, v[64:65]
	global_store_dword v[2:3], v14, off sc1
	v_lshl_add_u64 v[2:3], v[0:1], 0, v[66:67]
	global_store_dword v[2:3], v15, off sc1
	v_lshl_add_u64 v[2:3], v[0:1], 0, v[68:69]
	v_lshl_add_u64 v[0:1], v[0:1], 0, v[70:71]
	global_store_dword v[2:3], v16, off sc1
	global_store_dword v[0:1], v17, off sc1
	s_endpgm
